# prologue fp4 table conversion: one strided touch load of the next row per iteration so its 8 row loads hit L2
# baseline (speedup 1.0000x reference)
; #define GAS __attribute__((address_space(1)))
; __device__ __forceinline__ unsigned f2bf(float f) { unsigned u = __builtin_bit_cast(unsigned, f); return (u + 0x7fffu + ((u >> 16) & 1u)) >> 16; }
; __device__ __forceinline__ void row_to_fp4(const float* src, unsigned char* dst, size_t slice_stride, unsigned short* scale_out, int lane) {
;     f32x4 v[8]; float mx = 0.f;
; #pragma unroll
;     for (int q = 0; q < 8; ++q) { v[q] = ld_f4(src + q * 256 + lane * 4);
;         mx = fmaxf(mx, fmaxf(fmaxf(__builtin_fabsf(v[q][0]), __builtin_fabsf(v[q][1])), fmaxf(__builtin_fabsf(v[q][2]), __builtin_fabsf(v[q][3])))); }
; #pragma unroll
;     for (int o = 1; o < 64; o <<= 1) mx = fmaxf(mx, __shfl_xor(mx, o));
;     const float sc = mx > 0.f ? bf_lo(f2bf(mx * (1.0f / 6.0f)) ) : 1.0f, inv = 1.0f / sc;
; #pragma unroll
;     for (int q = 0; q < 8; ++q) { const f32x4 a = v[q] * inv;
;         unsigned w = 0u;
;         w = __builtin_amdgcn_cvt_scalef32_pk_fp4_f32(w, a[0], a[1], 1.0f, 0); w = __builtin_amdgcn_cvt_scalef32_pk_fp4_f32(w, a[2], a[3], 1.0f, 1);
;         *(GAS unsigned short*)(dst + (size_t)q * slice_stride + lane * 2) = (unsigned short)w; }
;     if (lane == 0) *(GAS unsigned short*)scale_out = (unsigned short)f2bf(sc);
; }
; __device__ __forceinline__ void p0_prologue(const Frame& F) {
;     ...
;         for (int r = F.gw; r < 2 * nrows; r += F.ngw) {
;             const bool isv = r >= nrows; const int rr = isv ? r - nrows : r;
;             row_to_fp4((isv ? F.peer_v : F.peer_u) + (size_t)rr * D, (isv ? VB : UB) + (size_t)(rr / NEXP) * NEXP * (D / 2) + (size_t)(rr % NEXP) * 128, (size_t)NEXP * 128, SUV + 2 * (size_t)rr + (isv ? 1 : 0), lane);
;         }
.LBB0_147:
	s_add_i32 s8, s21, 0xffff0000
	s_cmp_gt_i32 s21, 0xffff
	s_cselect_b64 s[2:3], -1, 0
	s_and_b64 s[6:7], s[2:3], exec
	s_cselect_b32 s6, s8, s21
	s_cselect_b32 s22, s59, s57
	s_cselect_b32 s23, s58, s56
	s_ashr_i32 s7, s6, 31
	s_lshl_b64 s[8:9], s[6:7], 13
	s_add_u32 s8, s23, s8
	s_addc_u32 s9, s22, s9
	v_lshl_add_u64 v[0:1], v[34:35], 2, s[8:9]
	global_load_dwordx4 v[28:31], v[0:1], off
	global_load_dwordx4 v[24:27], v[0:1], off offset:1024
	global_load_dwordx4 v[20:23], v[0:1], off offset:2048
	global_load_dwordx4 v[16:19], v[0:1], off offset:3072
	v_add_co_u32_e32 v0, vcc, s12, v0
	s_waitcnt vmcnt(3)
	v_max_f32_e64 v45, |v31|, |v31|
	v_addc_co_u32_e32 v1, vcc, 0, v1, vcc
	s_waitcnt lgkmcnt(0)
	global_load_dwordx4 v[12:15], v[0:1], off
	global_load_dwordx4 v[8:11], v[0:1], off offset:1024
	global_load_dwordx4 v[4:7], v[0:1], off offset:2048
	s_nop 0
	global_load_dwordx4 v[0:3], v[0:1], off offset:3072
	s_add_i32 s100, s21, s82
	s_cmp_gt_i32 s100, 0x1ffff
	s_cselect_b32 s100, s21, s100
	s_cmp_gt_i32 s100, 0xffff
	s_cselect_b32 s101, s59, s57
	v_mov_b32_e32 v61, s101
	s_cselect_b32 s101, s58, s56
	v_mov_b32_e32 v60, s101
	s_cselect_b32 s101, 0x10000, 0
	s_sub_i32 s100, s100, s101
	s_lshl_b32 s100, s100, 13
	v_lshl_add_u32 v62, v34, 5, s100
	v_add_co_u32_e32 v60, vcc, v60, v62
	s_nop 1
	v_addc_co_u32_e32 v61, vcc, 0, v61, vcc
	global_load_dword v62, v[60:61], off
	v_max_f32_e64 v46, |v30|, |v30|
	s_waitcnt vmcnt(7)
	v_max_f32_e64 v47, |v27|, |v27|
	v_max_f32_e64 v48, |v26|, |v26|
	s_waitcnt vmcnt(6)
	v_max_f32_e64 v49, |v23|, |v23|
	v_max_f32_e64 v50, |v22|, |v22|
	s_waitcnt vmcnt(5)
	v_max_f32_e64 v51, |v19|, |v19|
	v_max_f32_e64 v52, |v18|, |v18|
	v_max_f32_e32 v45, v46, v45
	v_max_f32_e32 v46, v48, v47
	v_max_f32_e32 v47, v50, v49
	v_max_f32_e32 v48, v52, v51
	v_max3_f32 v45, |v28|, |v29|, v45
	v_max3_f32 v46, |v24|, |v25|, v46
	v_max3_f32 v47, |v20|, |v21|, v47
	v_max3_f32 v48, |v16|, |v17|, v48
	v_max3_f32 v45, v45, 0, v46
	v_max3_f32 v45, v45, v47, v48
	s_waitcnt vmcnt(4)
	v_max_f32_e64 v49, |v15|, |v15|
	v_max_f32_e64 v50, |v14|, |v14|
	s_waitcnt vmcnt(3)
	v_max_f32_e64 v51, |v11|, |v11|
	v_max_f32_e64 v52, |v10|, |v10|
	s_waitcnt vmcnt(2)
	v_max_f32_e64 v53, |v7|, |v7|
	v_max_f32_e64 v54, |v6|, |v6|
	s_waitcnt vmcnt(1)
	v_max_f32_e64 v55, |v3|, |v3|
	v_max_f32_e64 v56, |v2|, |v2|
	v_max_f32_e32 v49, v50, v49
	v_max_f32_e32 v50, v52, v51
	v_max_f32_e32 v51, v54, v53
	v_max_f32_e32 v52, v56, v55
	v_max3_f32 v46, |v12|, |v13|, v49
	v_max3_f32 v49, |v8|, |v9|, v50
	v_max3_f32 v50, |v4|, |v5|, v51
	v_max3_f32 v51, |v0|, |v1|, v52
	v_max3_f32 v45, v45, v46, v49
	v_max3_f32 v45, v45, v50, v51
	s_waitcnt lgkmcnt(0)
	s_nop 1
	v_max_f32_dpp v45, v45, v45 quad_perm:[1,0,3,2] row_mask:0xf bank_mask:0xf
	s_nop 1
	v_max_f32_dpp v45, v45, v45 quad_perm:[2,3,0,1] row_mask:0xf bank_mask:0xf
	s_nop 1
	v_max_f32_dpp v45, v45, v45 row_half_mirror row_mask:0xf bank_mask:0xf
	s_nop 1
	v_max_f32_dpp v45, v45, v45 row_mirror row_mask:0xf bank_mask:0xf
	s_nop 1
	v_max_f32_dpp v45, v45, v45 row_bcast:15 row_mask:0xa bank_mask:0xf
	s_nop 1
	v_max_f32_dpp v45, v45, v45 row_bcast:31 row_mask:0xc bank_mask:0xf
	s_nop 1
	v_readlane_b32 s100, v45, 63
	s_nop 3
	v_mov_b32_e32 v45, s100
	v_mov_b32_e32 v46, s100
	s_waitcnt lgkmcnt(0)
; #define GAS __attribute__((address_space(1)))
; __device__ __forceinline__ unsigned f2bf(float f) { unsigned u = __builtin_bit_cast(unsigned, f); return (u + 0x7fffu + ((u >> 16) & 1u)) >> 16; }
; __device__ __forceinline__ unsigned pk2(float lo, float hi) { return f2bf(lo) | (f2bf(hi) << 16); }
; __device__ __forceinline__ void row_to_fp4(const float* src, unsigned char* dst, size_t slice_stride, unsigned short* scale_out, int lane) {
;     ...
;     const float sc = mx > 0.f ? bf_lo(f2bf(mx * (1.0f / 6.0f)) ) : 1.0f, inv = 1.0f / sc;
; #pragma unroll
;     for (int q = 0; q < 8; ++q) { const f32x4 a = v[q] * inv;
;         unsigned w = 0u;
;         w = __builtin_amdgcn_cvt_scalef32_pk_fp4_f32(w, a[0], a[1], 1.0f, 0); w = __builtin_amdgcn_cvt_scalef32_pk_fp4_f32(w, a[2], a[3], 1.0f, 1);
;         *(GAS unsigned short*)(dst + (size_t)q * slice_stride + lane * 2) = (unsigned short)w; }
;     if (lane == 0) *(GAS unsigned short*)scale_out = (unsigned short)f2bf(sc);
; }
; __device__ __forceinline__ void p0_prologue(const Frame& F) {
;     ...
;         const size_t nK = (size_t)DEPTH * 16 * 128 * 128 / 8;
;         bf16* KB = (bf16*)(F.ws + WS_KEYS);
;         const size_t stride = (size_t)F.ngw * 64, start = (size_t)F.gw * 64 + lane;
;         for (size_t i = start; i < nK; i += stride) {
;             const f32x4 a = ld_f4(F.peer_keys + i * 8), b = ld_f4(F.peer_keys + i * 8 + 4);
;             u32x4 o; o.x = pk2(a[0], a[1]); o.y = pk2(a[2], a[3]); o.z = pk2(b[0], b[1]); o.w = pk2(b[2], b[3]); st_u4(KB + i * 8, o);
	v_max_f32_e32 v46, v46, v46
	v_max_f32_e32 v46, v45, v46
	v_cmp_lt_f32_e32 vcc, 0, v46
	v_mov_b32_e32 v45, 1.0
	s_and_saveexec_b64 s[8:9], vcc
	v_mul_f32_e32 v45, 0x3e2aaaab, v46
	v_bfe_u32 v46, v45, 16, 1
	v_add3_u32 v45, v45, v46, s13
	v_and_b32_e32 v45, 0xffff0000, v45
	s_or_b64 exec, exec, s[8:9]
	s_and_b64 s[8:9], s[2:3], exec
	s_cselect_b32 s8, s14, 0x3b400000
	s_add_u32 s22, s62, s8
	s_addc_u32 s23, s63, 0
	s_lshr_b32 s8, s7, 18
	s_add_i32 s24, s6, s8
	s_ashr_i32 s8, s24, 14
	s_ashr_i32 s9, s8, 31
	s_lshl_b64 s[8:9], s[8:9], 24
	s_add_u32 s25, s22, s8
	s_addc_u32 s26, s23, s9
	v_div_scale_f32 v46, s[22:23], v45, v45, 1.0
	v_rcp_f32_e32 v47, v46
	s_and_b32 s8, s24, 0xffffc000
	s_sub_i32 s8, s6, s8
	s_ashr_i32 s9, s8, 31
	v_fma_f32 v48, -v46, v47, 1.0
	v_fmac_f32_e32 v47, v48, v47
	v_div_scale_f32 v48, vcc, 1.0, v45, 1.0
	v_mul_f32_e32 v49, v48, v47
	v_fma_f32 v50, -v46, v49, v48
	v_fmac_f32_e32 v49, v50, v47
	v_fma_f32 v46, -v46, v49, v48
	v_div_fmas_f32 v46, v46, v47, v49
	v_div_fixup_f32 v46, v46, v45, 1.0
	s_lshl_b64 s[8:9], s[8:9], 7
	v_pk_mul_f32 v[30:31], v[30:31], v[46:47] op_sel_hi:[1,0]
	v_pk_mul_f32 v[28:29], v[28:29], v[46:47] op_sel_hi:[1,0]
	v_mov_b32_e32 v47, 0
	s_add_u32 s8, s25, s8
	v_cvt_scalef32_pk_fp4_f32 v47, v28, v29, 1.0
	s_addc_u32 s9, s26, s9
	v_cvt_scalef32_pk_fp4_f32 v47, v30, v31, 1.0 op_sel:[0,0,1,0]
	v_lshl_add_u64 v[48:49], s[8:9], 0, v[36:37]
	v_pk_mul_f32 v[24:25], v[24:25], v[46:47] op_sel_hi:[1,0]
	v_mov_b32_e32 v28, 0
	v_pk_mul_f32 v[26:27], v[26:27], v[46:47] op_sel_hi:[1,0]
	v_cvt_scalef32_pk_fp4_f32 v28, v24, v25, 1.0
	v_add_co_u32_e32 v24, vcc, s15, v48
	v_cvt_scalef32_pk_fp4_f32 v28, v26, v27, 1.0 op_sel:[0,0,1,0]
	s_nop 0
	v_addc_co_u32_e32 v25, vcc, 0, v49, vcc
	global_store_short v[24:25], v28, off
	v_pk_mul_f32 v[20:21], v[20:21], v[46:47] op_sel_hi:[1,0]
	v_mov_b32_e32 v24, 0
	v_pk_mul_f32 v[22:23], v[22:23], v[46:47] op_sel_hi:[1,0]
	v_cvt_scalef32_pk_fp4_f32 v24, v20, v21, 1.0
	v_add_co_u32_e32 v20, vcc, s16, v48
	v_cvt_scalef32_pk_fp4_f32 v24, v22, v23, 1.0 op_sel:[0,0,1,0]
	s_nop 0
	v_addc_co_u32_e32 v21, vcc, 0, v49, vcc
	global_store_short v[20:21], v24, off
	v_pk_mul_f32 v[16:17], v[16:17], v[46:47] op_sel_hi:[1,0]
	v_mov_b32_e32 v20, 0
	v_pk_mul_f32 v[18:19], v[18:19], v[46:47] op_sel_hi:[1,0]
	v_cvt_scalef32_pk_fp4_f32 v20, v16, v17, 1.0
	v_add_co_u32_e32 v16, vcc, s17, v48
	v_cvt_scalef32_pk_fp4_f32 v20, v18, v19, 1.0 op_sel:[0,0,1,0]
	s_nop 0
	v_addc_co_u32_e32 v17, vcc, 0, v49, vcc
	global_store_short v[16:17], v20, off
	v_pk_mul_f32 v[12:13], v[12:13], v[46:47] op_sel_hi:[1,0]
	v_mov_b32_e32 v16, 0
	v_pk_mul_f32 v[14:15], v[14:15], v[46:47] op_sel_hi:[1,0]
	v_cvt_scalef32_pk_fp4_f32 v16, v12, v13, 1.0
	v_add_co_u32_e32 v12, vcc, s18, v48
	v_cvt_scalef32_pk_fp4_f32 v16, v14, v15, 1.0 op_sel:[0,0,1,0]
	s_nop 0
	v_addc_co_u32_e32 v13, vcc, 0, v49, vcc
	global_store_short v[12:13], v16, off
	v_pk_mul_f32 v[8:9], v[8:9], v[46:47] op_sel_hi:[1,0]
	v_mov_b32_e32 v12, 0
	v_pk_mul_f32 v[10:11], v[10:11], v[46:47] op_sel_hi:[1,0]
	v_cvt_scalef32_pk_fp4_f32 v12, v8, v9, 1.0
	v_add_co_u32_e32 v8, vcc, s19, v48
	v_cvt_scalef32_pk_fp4_f32 v12, v10, v11, 1.0 op_sel:[0,0,1,0]
	s_nop 0
	v_addc_co_u32_e32 v9, vcc, 0, v49, vcc
	global_store_short v[8:9], v12, off
	v_pk_mul_f32 v[4:5], v[4:5], v[46:47] op_sel_hi:[1,0]
	v_mov_b32_e32 v8, 0
	v_pk_mul_f32 v[6:7], v[6:7], v[46:47] op_sel_hi:[1,0]
	v_cvt_scalef32_pk_fp4_f32 v8, v4, v5, 1.0
	v_add_co_u32_e32 v4, vcc, s20, v48
	v_cvt_scalef32_pk_fp4_f32 v8, v6, v7, 1.0 op_sel:[0,0,1,0]
	s_nop 0
	v_addc_co_u32_e32 v5, vcc, 0, v49, vcc
	global_store_short v[4:5], v8, off
	v_pk_mul_f32 v[0:1], v[0:1], v[46:47] op_sel_hi:[1,0]
	v_mov_b32_e32 v4, 0
	v_pk_mul_f32 v[2:3], v[2:3], v[46:47] op_sel_hi:[1,0]
	v_cvt_scalef32_pk_fp4_f32 v4, v0, v1, 1.0
	v_add_co_u32_e32 v0, vcc, 0xe00000, v48
	v_cvt_scalef32_pk_fp4_f32 v4, v2, v3, 1.0 op_sel:[0,0,1,0]
	s_nop 0
	v_addc_co_u32_e32 v1, vcc, 0, v49, vcc
	global_store_short v[48:49], v47, off
	global_store_short v[0:1], v4, off
	s_and_saveexec_b64 s[8:9], s[0:1]
	s_cbranch_execz .LBB0_146
	s_lshl_b64 s[6:7], s[6:7], 2
	s_add_u32 s6, s10, s6
	v_cndmask_b32_e64 v0, 0, 1, s[2:3]
	v_bfe_u32 v1, v45, 16, 1
	s_addc_u32 s7, s11, s7
	v_lshlrev_b32_e32 v0, 1, v0
	v_add3_u32 v1, v45, v1, s13
	global_store_short_d16_hi v0, v1, s[6:7]
	s_branch .LBB0_146
.LBB0_151:
	s_waitcnt vmcnt(0)
	s_lshl_b64 s[0:1], s[94:95], 6
	v_ashrrev_i32_e32 v33, 31, v32
	v_lshl_add_u64 v[0:1], s[0:1], 0, v[32:33]
	s_mov_b64 s[0:1], 0x20000
	v_cmp_gt_u64_e32 vcc, s[0:1], v[0:1]
	s_and_saveexec_b64 s[0:1], vcc
	s_cbranch_execz .LBB0_154
	s_lshl_b64 s[2:3], s[82:83], 6
	s_lshl_b64 s[6:7], s[94:95], 11
	s_add_u32 s6, s54, s6
	v_lshlrev_b64 v[2:3], 5, v[32:33]
	s_addc_u32 s7, s55, s7
	v_lshl_add_u64 v[2:3], s[6:7], 0, v[2:3]
	s_lshl_b64 s[6:7], s[82:83], 11
	s_lshl_b64 s[8:9], s[94:95], 10
	s_add_u32 s8, s62, s8
	s_addc_u32 s9, s63, s9
	v_lshl_add_u64 v[4:5], v[32:33], 4, s[8:9]
	s_mov_b64 s[8:9], 0x300000
	v_lshl_add_u64 v[2:3], v[2:3], 0, 16
	v_lshl_add_u64 v[4:5], v[4:5], 0, s[8:9]
	s_lshl_b64 s[8:9], s[82:83], 10
	s_mov_b64 s[10:11], 0
	s_movk_i32 s14, 0x7fff
	s_mov_b32 s15, 0xffff0000
	s_mov_b64 s[12:13], 0x1ffff
